# scan: state-owning waves at s_setprio 3 over their staging partners on the same SIMD
# speedup vs baseline: 1.0196x; 1.0196x over previous
; #define LAS __attribute__((address_space(3)))
; __device__ __forceinline__ void p5_scan_block(Frame& F, int sb) {
;     ...
;     for (int c = 0; c < NCH; ++c) {
;         if (F.wave < 4) {
;             const LAS float* p = inb + (c & 1) * (SC_T * 384) + 4 * q; LAS float* yo = yb + (c & 1) * (SC_T * 16) + rloc;
;             const LAS float* pv = inb + (c & 1) * (SC_T * 384) + 192 + rg * 16 + rloc;
;             f32x4 w4 = *(const LAS f32x4*)(p), r4 = *(const LAS f32x4*)(p + 64), k4 = *(const LAS f32x4*)(p + 128), a4 = *(const LAS f32x4*)(p + 256), b4 = *(const LAS f32x4*)(p + 320); float vv = pv[0];
;             f32x4 w5 = *(const LAS f32x4*)(p + 384), r5 = *(const LAS f32x4*)(p + 384 + 64), k5 = *(const LAS f32x4*)(p + 384 + 128), a5 = *(const LAS f32x4*)(p + 384 + 256), b5 = *(const LAS f32x4*)(p + 384 + 320); float v5 = pv[384];
;             float yp[16];
; #pragma unroll
;             for (int s = 0; s < SC_T; ++s) {
;                 f32x4 nw = w5, nr = r5, nk = k5, na = a5, nb = b5; float nv = v5;
;                 if (s + 2 < SC_T) { nw = *(const LAS f32x4*)(p + (s + 2) * 384); nr = *(const LAS f32x4*)(p + (s + 2) * 384 + 64); nk = *(const LAS f32x4*)(p + (s + 2) * 384 + 128);
;                     na = *(const LAS f32x4*)(p + (s + 2) * 384 + 256); nb = *(const LAS f32x4*)(p + (s + 2) * 384 + 320); nv = pv[(s + 2) * 384]; }
;                 const f32x2 pa = Sa * a4.lo + Sb * a4.hi;
;                 float sa = pa.x + pa.y;
;                 const f32x2 ta = Sa * w4.lo + k4.lo * vv, tb = Sb * w4.hi + k4.hi * vv;
;                 sa = dpp_add16(sa);
;                 Sa = ta + b4.lo * sa; Sb = tb + b4.hi * sa;
;                 const f32x2 py = Sa * r4.lo + Sb * r4.hi;
;                 yp[s & 15] = py.x + py.y;
.LBB0_2786:
	s_setprio 3
	s_and_b32 s44, s31, 1
	s_mul_i32 s45, s44, 0xc000
	s_add_i32 s45, s45, 0
	v_lshl_add_u32 v150, v133, 2, s45
	s_add_i32 s45, s45, s35
	v_lshl_add_u32 v151, v95, 2, s45
	s_waitcnt vmcnt(6)
	ds_read_b128 v[34:37], v150
	s_waitcnt vmcnt(5)
	ds_read_b128 v[38:41], v150 offset:256
	s_waitcnt vmcnt(4)
	ds_read_b128 v[42:45], v150 offset:512
	s_waitcnt vmcnt(3)
	ds_read_b128 v[46:49], v150 offset:1024
	ds_read2st64_b32 v[124:125], v151 offset0:3 offset1:9
	s_waitcnt vmcnt(2)
	ds_read_b128 v[50:53], v150 offset:1280
	s_waitcnt vmcnt(1)
	ds_read_b128 v[54:57], v150 offset:1536
	s_waitcnt vmcnt(0)
	ds_read_b128 v[58:61], v150 offset:1792
	ds_read_b128 v[62:65], v150 offset:2048
	ds_read_b128 v[70:73], v150 offset:2560
	ds_read_b128 v[74:77], v150 offset:2816
	ds_read_b128 v[78:81], v150 offset:3072
	ds_read_b128 v[82:85], v150 offset:3328
	ds_read_b128 v[86:89], v150 offset:3584
	ds_read_b128 v[90:93], v150 offset:4096
	ds_read2st64_b32 v[126:127], v151 offset0:15 offset1:21
	s_waitcnt lgkmcnt(12)
	v_pk_mul_f32 v[46:47], v[66:67], v[46:47]
	s_waitcnt lgkmcnt(11)
	v_pk_mul_f32 v[42:43], v[42:43], v[124:125] op_sel_hi:[1,0]
	v_pk_fma_f32 v[46:47], v[68:69], v[48:49], v[46:47]
	v_pk_fma_f32 v[34:35], v[66:67], v[34:35], v[42:43]
	v_add_f32_e32 v46, v46, v47
	v_pk_mul_f32 v[42:43], v[44:45], v[124:125] op_sel_hi:[1,0]
	s_nop 0
	v_pk_fma_f32 v[36:37], v[68:69], v[36:37], v[42:43]
	v_add_f32_dpp v42, v46, v46 quad_perm:[1,0,3,2] row_mask:0xf bank_mask:0xf bound_ctrl:1
	s_nop 1
	v_add_f32_dpp v42, v42, v42 quad_perm:[2,3,0,1] row_mask:0xf bank_mask:0xf bound_ctrl:1
	s_nop 1
	v_add_f32_dpp v42, v42, v42 row_half_mirror row_mask:0xf bank_mask:0xf bound_ctrl:1
	s_nop 1
	v_add_f32_dpp v42, v42, v42 row_mirror row_mask:0xf bank_mask:0xf bound_ctrl:1
	s_waitcnt lgkmcnt(10)
	v_pk_fma_f32 v[152:153], v[50:51], v[42:43], v[34:35] op_sel_hi:[1,0,1]
	v_pk_fma_f32 v[52:53], v[52:53], v[42:43], v[36:37] op_sel_hi:[1,0,1]
	s_waitcnt lgkmcnt(6)
	v_pk_mul_f32 v[70:71], v[70:71], v[152:153]
	v_pk_mul_f32 v[34:35], v[40:41], v[52:53]
	v_pk_fma_f32 v[70:71], v[72:73], v[52:53], v[70:71]
	v_pk_fma_f32 v[34:35], v[38:39], v[152:153], v[34:35]
	v_pk_mul_f32 v[54:55], v[54:55], v[152:153]
	v_add_f32_e32 v34, v34, v35
	v_add_f32_e32 v35, v70, v71
	v_mov_b32_e32 v70, v125
	v_pk_fma_f32 v[54:55], v[62:63], v[70:71], v[54:55] op_sel_hi:[1,0,1]
	v_add_f32_dpp v35, v35, v35 quad_perm:[1,0,3,2] row_mask:0xf bank_mask:0xf bound_ctrl:1
	v_pk_mul_f32 v[52:53], v[56:57], v[52:53]
	ds_read_b128 v[36:39], v150 offset:4352
	ds_read_b128 v[40:43], v150 offset:4608
	ds_read_b128 v[44:47], v150 offset:4864
	ds_read_b128 v[48:51], v150 offset:5120
	ds_read_b128 v[66:69], v150 offset:5632
	ds_read_b128 v[120:123], v150 offset:5888
	v_add_f32_dpp v35, v35, v35 quad_perm:[2,3,0,1] row_mask:0xf bank_mask:0xf bound_ctrl:1
	v_pk_fma_f32 v[52:53], v[64:65], v[70:71], v[52:53] op_sel_hi:[1,0,1]
	s_nop 0
	v_add_f32_dpp v35, v35, v35 row_half_mirror row_mask:0xf bank_mask:0xf bound_ctrl:1
	s_nop 1
	v_add_f32_dpp v56, v35, v35 row_mirror row_mask:0xf bank_mask:0xf bound_ctrl:1
	s_waitcnt lgkmcnt(11)
	v_pk_fma_f32 v[64:65], v[74:75], v[56:57], v[54:55] op_sel_hi:[1,0,1]
	v_pk_fma_f32 v[74:75], v[76:77], v[56:57], v[52:53] op_sel_hi:[1,0,1]
	s_waitcnt lgkmcnt(7)
	v_pk_mul_f32 v[76:77], v[90:91], v[64:65]
	v_pk_mul_f32 v[52:53], v[60:61], v[74:75]
	v_pk_fma_f32 v[76:77], v[92:93], v[74:75], v[76:77]
	v_pk_fma_f32 v[52:53], v[58:59], v[64:65], v[52:53]
	v_add_f32_e32 v76, v76, v77
	v_pk_mul_f32 v[64:65], v[78:79], v[64:65]
	v_pk_mul_f32 v[74:75], v[80:81], v[74:75]
	v_add_f32_dpp v76, v76, v76 quad_perm:[1,0,3,2] row_mask:0xf bank_mask:0xf bound_ctrl:1
	s_waitcnt lgkmcnt(6)
	v_pk_fma_f32 v[64:65], v[86:87], v[126:127], v[64:65] op_sel_hi:[1,0,1]
	v_pk_fma_f32 v[74:75], v[88:89], v[126:127], v[74:75] op_sel_hi:[1,0,1]
	v_add_f32_dpp v76, v76, v76 quad_perm:[2,3,0,1] row_mask:0xf bank_mask:0xf bound_ctrl:1
	v_add_f32_e32 v35, v52, v53
	ds_read_b128 v[52:55], v150 offset:6144
	ds_read_b128 v[56:59], v150 offset:6400
	ds_read_b128 v[60:63], v150 offset:6656
	ds_read_b128 v[70:73], v150 offset:7168
	ds_read2st64_b32 v[124:125], v151 offset0:27 offset1:33
	v_add_f32_dpp v76, v76, v76 row_half_mirror row_mask:0xf bank_mask:0xf bound_ctrl:1
	s_nop 1
	v_add_f32_dpp v76, v76, v76 row_mirror row_mask:0xf bank_mask:0xf bound_ctrl:1
	s_waitcnt lgkmcnt(10)
	v_pk_fma_f32 v[64:65], v[36:37], v[76:77], v[64:65] op_sel_hi:[1,0,1]
	v_pk_fma_f32 v[152:153], v[38:39], v[76:77], v[74:75] op_sel_hi:[1,0,1]
	s_waitcnt lgkmcnt(6)
	v_pk_mul_f32 v[66:67], v[66:67], v[64:65]
	v_pk_mul_f32 v[36:37], v[84:85], v[152:153]
	v_pk_fma_f32 v[66:67], v[68:69], v[152:153], v[66:67]
	v_pk_fma_f32 v[36:37], v[82:83], v[64:65], v[36:37]
	v_add_f32_e32 v66, v66, v67
	v_pk_mul_f32 v[40:41], v[40:41], v[64:65]
	v_mov_b32_e32 v64, v127
	v_pk_fma_f32 v[40:41], v[48:49], v[64:65], v[40:41] op_sel_hi:[1,0,1]
	v_add_f32_dpp v48, v66, v66 quad_perm:[1,0,3,2] row_mask:0xf bank_mask:0xf bound_ctrl:1
	v_pk_mul_f32 v[42:43], v[42:43], v[152:153]
	v_add_f32_e32 v154, v36, v37
	v_add_f32_dpp v48, v48, v48 quad_perm:[2,3,0,1] row_mask:0xf bank_mask:0xf bound_ctrl:1
	v_pk_fma_f32 v[42:43], v[50:51], v[64:65], v[42:43] op_sel_hi:[1,0,1]
	ds_read_b128 v[36:39], v150 offset:7424
	ds_read_b128 v[74:77], v150 offset:7680
	ds_read_b128 v[78:81], v150 offset:7936
	ds_read_b128 v[82:85], v150 offset:8192
	ds_read_b128 v[86:89], v150 offset:8704
	ds_read_b128 v[90:93], v150 offset:8960
	v_add_f32_dpp v48, v48, v48 row_half_mirror row_mask:0xf bank_mask:0xf bound_ctrl:1
	s_nop 1
	v_add_f32_dpp v48, v48, v48 row_mirror row_mask:0xf bank_mask:0xf bound_ctrl:1
	s_waitcnt lgkmcnt(11)
; #define LAS __attribute__((address_space(3)))
; __device__ __forceinline__ void p5_scan_block(Frame& F, int sb) {
;     ...
;             for (int s = 0; s < SC_T; ++s) {
;                 f32x4 nw = w5, nr = r5, nk = k5, na = a5, nb = b5; float nv = v5;
;                 if (s + 2 < SC_T) { nw = *(const LAS f32x4*)(p + (s + 2) * 384); nr = *(const LAS f32x4*)(p + (s + 2) * 384 + 64); nk = *(const LAS f32x4*)(p + (s + 2) * 384 + 128);
;                     na = *(const LAS f32x4*)(p + (s + 2) * 384 + 256); nb = *(const LAS f32x4*)(p + (s + 2) * 384 + 320); nv = pv[(s + 2) * 384]; }
;                 const f32x2 pa = Sa * a4.lo + Sb * a4.hi;
;                 float sa = pa.x + pa.y;
;                 const f32x2 ta = Sa * w4.lo + k4.lo * vv, tb = Sb * w4.hi + k4.hi * vv;
;                 sa = dpp_add16(sa);
;                 Sa = ta + b4.lo * sa; Sb = tb + b4.hi * sa;
;                 const f32x2 py = Sa * r4.lo + Sb * r4.hi;
;                 yp[s & 15] = py.x + py.y;
	v_pk_fma_f32 v[68:69], v[120:121], v[48:49], v[40:41] op_sel_hi:[1,0,1]
	v_pk_fma_f32 v[120:121], v[122:123], v[48:49], v[42:43] op_sel_hi:[1,0,1]
	s_waitcnt lgkmcnt(7)
	v_pk_mul_f32 v[70:71], v[70:71], v[68:69]
	v_pk_mul_f32 v[52:53], v[52:53], v[68:69]
	v_pk_fma_f32 v[70:71], v[72:73], v[120:121], v[70:71]
	s_waitcnt lgkmcnt(6)
	v_pk_fma_f32 v[52:53], v[60:61], v[124:125], v[52:53] op_sel_hi:[1,0,1]
	v_add_f32_e32 v70, v70, v71
	v_pk_mul_f32 v[54:55], v[54:55], v[120:121]
	v_pk_mul_f32 v[40:41], v[46:47], v[120:121]
	v_add_f32_dpp v60, v70, v70 quad_perm:[1,0,3,2] row_mask:0xf bank_mask:0xf bound_ctrl:1
	v_pk_fma_f32 v[54:55], v[62:63], v[124:125], v[54:55] op_sel_hi:[1,0,1]
	v_pk_fma_f32 v[40:41], v[44:45], v[68:69], v[40:41]
	v_add_f32_dpp v60, v60, v60 quad_perm:[2,3,0,1] row_mask:0xf bank_mask:0xf bound_ctrl:1
	v_add_f32_e32 v155, v40, v41
	ds_read_b128 v[40:43], v150 offset:9216
	ds_read_b128 v[44:47], v150 offset:9472
	ds_read_b128 v[48:51], v150 offset:9728
	ds_read_b128 v[64:67], v150 offset:10240
	ds_read2st64_b32 v[126:127], v151 offset0:39 offset1:45
	v_add_f32_dpp v60, v60, v60 row_half_mirror row_mask:0xf bank_mask:0xf bound_ctrl:1
	s_nop 1
	v_add_f32_dpp v60, v60, v60 row_mirror row_mask:0xf bank_mask:0xf bound_ctrl:1
	s_waitcnt lgkmcnt(10)
	v_pk_fma_f32 v[72:73], v[36:37], v[60:61], v[52:53] op_sel_hi:[1,0,1]
	v_pk_fma_f32 v[152:153], v[38:39], v[60:61], v[54:55] op_sel_hi:[1,0,1]
	s_waitcnt lgkmcnt(6)
	v_pk_mul_f32 v[86:87], v[86:87], v[72:73]
	v_pk_mul_f32 v[36:37], v[58:59], v[152:153]
	v_pk_fma_f32 v[86:87], v[88:89], v[152:153], v[86:87]
	v_pk_fma_f32 v[36:37], v[56:57], v[72:73], v[36:37]
	v_add_f32_e32 v86, v86, v87
	v_pk_mul_f32 v[72:73], v[74:75], v[72:73]
	v_mov_b32_e32 v74, v125
	v_pk_mul_f32 v[76:77], v[76:77], v[152:153]
	v_pk_fma_f32 v[72:73], v[82:83], v[74:75], v[72:73] op_sel_hi:[1,0,1]
	v_pk_fma_f32 v[74:75], v[84:85], v[74:75], v[76:77] op_sel_hi:[1,0,1]
	v_add_f32_dpp v76, v86, v86 quad_perm:[1,0,3,2] row_mask:0xf bank_mask:0xf bound_ctrl:1
	v_add_f32_e32 v156, v36, v37
	ds_read_b128 v[36:39], v150 offset:10496
	ds_read_b128 v[52:55], v150 offset:10752
	ds_read_b128 v[56:59], v150 offset:11008
	ds_read_b128 v[60:63], v150 offset:11264
	ds_read_b128 v[68:71], v150 offset:11776
	ds_read_b128 v[120:123], v150 offset:12032
	v_add_f32_dpp v76, v76, v76 quad_perm:[2,3,0,1] row_mask:0xf bank_mask:0xf bound_ctrl:1
	s_nop 1
	v_add_f32_dpp v76, v76, v76 row_half_mirror row_mask:0xf bank_mask:0xf bound_ctrl:1
	s_nop 1
	v_add_f32_dpp v76, v76, v76 row_mirror row_mask:0xf bank_mask:0xf bound_ctrl:1
	s_waitcnt lgkmcnt(11)
	v_pk_fma_f32 v[88:89], v[90:91], v[76:77], v[72:73] op_sel_hi:[1,0,1]
	v_pk_fma_f32 v[90:91], v[92:93], v[76:77], v[74:75] op_sel_hi:[1,0,1]
	s_waitcnt lgkmcnt(7)
	v_pk_mul_f32 v[64:65], v[64:65], v[88:89]
	v_pk_mul_f32 v[40:41], v[40:41], v[88:89]
	v_pk_fma_f32 v[64:65], v[66:67], v[90:91], v[64:65]
	s_waitcnt lgkmcnt(6)
	v_pk_fma_f32 v[40:41], v[48:49], v[126:127], v[40:41] op_sel_hi:[1,0,1]
	v_add_f32_e32 v64, v64, v65
	v_pk_mul_f32 v[42:43], v[42:43], v[90:91]
	v_pk_mul_f32 v[72:73], v[80:81], v[90:91]
	v_add_f32_dpp v48, v64, v64 quad_perm:[1,0,3,2] row_mask:0xf bank_mask:0xf bound_ctrl:1
	v_pk_fma_f32 v[42:43], v[50:51], v[126:127], v[42:43] op_sel_hi:[1,0,1]
	v_pk_fma_f32 v[72:73], v[78:79], v[88:89], v[72:73]
	v_add_f32_dpp v48, v48, v48 quad_perm:[2,3,0,1] row_mask:0xf bank_mask:0xf bound_ctrl:1
	v_add_f32_e32 v157, v72, v73
	ds_read_b128 v[72:75], v150 offset:12288
	ds_read_b128 v[76:79], v150 offset:12544
	ds_read_b128 v[80:83], v150 offset:12800
	ds_read_b128 v[84:87], v150 offset:13312
	ds_read2st64_b32 v[92:93], v151 offset0:51 offset1:57
	v_add_f32_dpp v48, v48, v48 row_half_mirror row_mask:0xf bank_mask:0xf bound_ctrl:1
	s_nop 1
	v_add_f32_dpp v48, v48, v48 row_mirror row_mask:0xf bank_mask:0xf bound_ctrl:1
	s_waitcnt lgkmcnt(10)
	v_pk_fma_f32 v[124:125], v[36:37], v[48:49], v[40:41] op_sel_hi:[1,0,1]
	v_pk_fma_f32 v[152:153], v[38:39], v[48:49], v[42:43] op_sel_hi:[1,0,1]
	s_waitcnt lgkmcnt(6)
	v_pk_mul_f32 v[68:69], v[68:69], v[124:125]
	v_pk_mul_f32 v[52:53], v[52:53], v[124:125]
	v_pk_fma_f32 v[68:69], v[70:71], v[152:153], v[68:69]
	v_pk_mul_f32 v[54:55], v[54:55], v[152:153]
	v_add_f32_e32 v69, v68, v69
	v_mov_b32_e32 v68, v127
	v_pk_fma_f32 v[52:53], v[60:61], v[68:69], v[52:53] op_sel_hi:[1,0,1]
	v_add_f32_dpp v60, v69, v69 quad_perm:[1,0,3,2] row_mask:0xf bank_mask:0xf bound_ctrl:1
	v_pk_fma_f32 v[54:55], v[62:63], v[68:69], v[54:55] op_sel_hi:[1,0,1]
	v_pk_mul_f32 v[36:37], v[46:47], v[152:153]
	v_add_f32_dpp v60, v60, v60 quad_perm:[2,3,0,1] row_mask:0xf bank_mask:0xf bound_ctrl:1
	v_pk_fma_f32 v[36:37], v[44:45], v[124:125], v[36:37]
	s_nop 0
	v_add_f32_dpp v60, v60, v60 row_half_mirror row_mask:0xf bank_mask:0xf bound_ctrl:1
	v_add_f32_e32 v158, v36, v37
	ds_read_b128 v[36:39], v150 offset:13568
	ds_read_b128 v[40:43], v150 offset:13824
	ds_read_b128 v[44:47], v150 offset:14080
	ds_read_b128 v[48:51], v150 offset:14336
	ds_read_b128 v[64:67], v150 offset:14848
	ds_read_b128 v[88:91], v150 offset:15104
	v_add_f32_dpp v60, v60, v60 row_mirror row_mask:0xf bank_mask:0xf bound_ctrl:1
	s_waitcnt lgkmcnt(11)
	v_pk_fma_f32 v[120:121], v[120:121], v[60:61], v[52:53] op_sel_hi:[1,0,1]
	v_pk_fma_f32 v[122:123], v[122:123], v[60:61], v[54:55] op_sel_hi:[1,0,1]
	s_waitcnt lgkmcnt(7)
	v_pk_mul_f32 v[84:85], v[84:85], v[120:121]
	v_pk_mul_f32 v[72:73], v[72:73], v[120:121]
	v_pk_fma_f32 v[84:85], v[86:87], v[122:123], v[84:85]
	s_waitcnt lgkmcnt(6)
; #define LAS __attribute__((address_space(3)))
; __device__ __forceinline__ void p5_scan_block(Frame& F, int sb) {
;     ...
;             for (int s = 0; s < SC_T; ++s) {
;                 f32x4 nw = w5, nr = r5, nk = k5, na = a5, nb = b5; float nv = v5;
;                 if (s + 2 < SC_T) { nw = *(const LAS f32x4*)(p + (s + 2) * 384); nr = *(const LAS f32x4*)(p + (s + 2) * 384 + 64); nk = *(const LAS f32x4*)(p + (s + 2) * 384 + 128);
;                     na = *(const LAS f32x4*)(p + (s + 2) * 384 + 256); nb = *(const LAS f32x4*)(p + (s + 2) * 384 + 320); nv = pv[(s + 2) * 384]; }
;                 const f32x2 pa = Sa * a4.lo + Sb * a4.hi;
;                 float sa = pa.x + pa.y;
;                 const f32x2 ta = Sa * w4.lo + k4.lo * vv, tb = Sb * w4.hi + k4.hi * vv;
;                 sa = dpp_add16(sa);
;                 Sa = ta + b4.lo * sa; Sb = tb + b4.hi * sa;
;                 const f32x2 py = Sa * r4.lo + Sb * r4.hi;
;                 yp[s & 15] = py.x + py.y;
	v_pk_fma_f32 v[72:73], v[80:81], v[92:93], v[72:73] op_sel_hi:[1,0,1]
	v_add_f32_e32 v84, v84, v85
	v_pk_mul_f32 v[74:75], v[74:75], v[122:123]
	v_pk_mul_f32 v[52:53], v[58:59], v[122:123]
	v_add_f32_dpp v80, v84, v84 quad_perm:[1,0,3,2] row_mask:0xf bank_mask:0xf bound_ctrl:1
	v_pk_fma_f32 v[74:75], v[82:83], v[92:93], v[74:75] op_sel_hi:[1,0,1]
	v_pk_fma_f32 v[52:53], v[56:57], v[120:121], v[52:53]
	v_add_f32_dpp v80, v80, v80 quad_perm:[2,3,0,1] row_mask:0xf bank_mask:0xf bound_ctrl:1
	v_add_f32_e32 v159, v52, v53
	ds_read_b128 v[52:55], v150 offset:15360
	ds_read_b128 v[56:59], v150 offset:15616
	ds_read_b128 v[60:63], v150 offset:15872
	ds_read_b128 v[68:71], v150 offset:16384
	ds_read2st64_b32 v[124:125], v151 offset0:63 offset1:69
	v_add_f32_dpp v80, v80, v80 row_half_mirror row_mask:0xf bank_mask:0xf bound_ctrl:1
	s_nop 1
	v_add_f32_dpp v80, v80, v80 row_mirror row_mask:0xf bank_mask:0xf bound_ctrl:1
	s_waitcnt lgkmcnt(10)
	v_pk_fma_f32 v[126:127], v[36:37], v[80:81], v[72:73] op_sel_hi:[1,0,1]
	v_pk_fma_f32 v[152:153], v[38:39], v[80:81], v[74:75] op_sel_hi:[1,0,1]
	s_waitcnt lgkmcnt(6)
	v_pk_mul_f32 v[64:65], v[64:65], v[126:127]
	v_pk_mul_f32 v[40:41], v[40:41], v[126:127]
	v_pk_fma_f32 v[64:65], v[66:67], v[152:153], v[64:65]
	v_pk_mul_f32 v[42:43], v[42:43], v[152:153]
	v_add_f32_e32 v65, v64, v65
	v_mov_b32_e32 v64, v93
	v_pk_fma_f32 v[40:41], v[48:49], v[64:65], v[40:41] op_sel_hi:[1,0,1]
	v_add_f32_dpp v48, v65, v65 quad_perm:[1,0,3,2] row_mask:0xf bank_mask:0xf bound_ctrl:1
	v_pk_fma_f32 v[42:43], v[50:51], v[64:65], v[42:43] op_sel_hi:[1,0,1]
	v_pk_mul_f32 v[36:37], v[78:79], v[152:153]
	v_add_f32_dpp v48, v48, v48 quad_perm:[2,3,0,1] row_mask:0xf bank_mask:0xf bound_ctrl:1
	v_pk_fma_f32 v[36:37], v[76:77], v[126:127], v[36:37]
	s_nop 0
	v_add_f32_dpp v48, v48, v48 row_half_mirror row_mask:0xf bank_mask:0xf bound_ctrl:1
	v_add_f32_e32 v160, v36, v37
	ds_read_b128 v[36:39], v150 offset:16640
	ds_read_b128 v[72:75], v150 offset:16896
	ds_read_b128 v[76:79], v150 offset:17152
	ds_read_b128 v[80:83], v150 offset:17408
	ds_read_b128 v[84:87], v150 offset:17920
	ds_read_b128 v[120:123], v150 offset:18176
	v_add_f32_dpp v48, v48, v48 row_mirror row_mask:0xf bank_mask:0xf bound_ctrl:1
	s_waitcnt lgkmcnt(11)
	v_pk_fma_f32 v[88:89], v[88:89], v[48:49], v[40:41] op_sel_hi:[1,0,1]
	v_pk_fma_f32 v[90:91], v[90:91], v[48:49], v[42:43] op_sel_hi:[1,0,1]
	s_waitcnt lgkmcnt(7)
	v_pk_mul_f32 v[68:69], v[68:69], v[88:89]
	v_pk_mul_f32 v[52:53], v[52:53], v[88:89]
	v_pk_fma_f32 v[68:69], v[70:71], v[90:91], v[68:69]
	s_waitcnt lgkmcnt(6)
	v_pk_fma_f32 v[52:53], v[60:61], v[124:125], v[52:53] op_sel_hi:[1,0,1]
	v_add_f32_e32 v68, v68, v69
	v_pk_mul_f32 v[54:55], v[54:55], v[90:91]
	v_pk_mul_f32 v[40:41], v[46:47], v[90:91]
	v_add_f32_dpp v60, v68, v68 quad_perm:[1,0,3,2] row_mask:0xf bank_mask:0xf bound_ctrl:1
	v_pk_fma_f32 v[54:55], v[62:63], v[124:125], v[54:55] op_sel_hi:[1,0,1]
	v_pk_fma_f32 v[40:41], v[44:45], v[88:89], v[40:41]
	v_add_f32_dpp v60, v60, v60 quad_perm:[2,3,0,1] row_mask:0xf bank_mask:0xf bound_ctrl:1
	v_add_f32_e32 v161, v40, v41
	ds_read_b128 v[40:43], v150 offset:18432
	ds_read_b128 v[44:47], v150 offset:18688
	ds_read_b128 v[48:51], v150 offset:18944
	ds_read_b128 v[64:67], v150 offset:19456
	ds_read2st64_b32 v[92:93], v151 offset0:75 offset1:81
	v_add_f32_dpp v60, v60, v60 row_half_mirror row_mask:0xf bank_mask:0xf bound_ctrl:1
	s_nop 1
	v_add_f32_dpp v60, v60, v60 row_mirror row_mask:0xf bank_mask:0xf bound_ctrl:1
	s_waitcnt lgkmcnt(10)
	v_pk_fma_f32 v[126:127], v[36:37], v[60:61], v[52:53] op_sel_hi:[1,0,1]
	v_pk_fma_f32 v[152:153], v[38:39], v[60:61], v[54:55] op_sel_hi:[1,0,1]
	s_waitcnt lgkmcnt(6)
	v_pk_mul_f32 v[84:85], v[84:85], v[126:127]
	v_pk_mul_f32 v[72:73], v[72:73], v[126:127]
	v_pk_fma_f32 v[84:85], v[86:87], v[152:153], v[84:85]
	v_pk_mul_f32 v[74:75], v[74:75], v[152:153]
	v_add_f32_e32 v85, v84, v85
	v_mov_b32_e32 v84, v125
	v_pk_fma_f32 v[72:73], v[80:81], v[84:85], v[72:73] op_sel_hi:[1,0,1]
	v_add_f32_dpp v80, v85, v85 quad_perm:[1,0,3,2] row_mask:0xf bank_mask:0xf bound_ctrl:1
	v_pk_fma_f32 v[74:75], v[82:83], v[84:85], v[74:75] op_sel_hi:[1,0,1]
	v_pk_mul_f32 v[36:37], v[58:59], v[152:153]
	v_add_f32_dpp v80, v80, v80 quad_perm:[2,3,0,1] row_mask:0xf bank_mask:0xf bound_ctrl:1
	v_pk_fma_f32 v[36:37], v[56:57], v[126:127], v[36:37]
	s_nop 0
	v_add_f32_dpp v80, v80, v80 row_half_mirror row_mask:0xf bank_mask:0xf bound_ctrl:1
	v_add_f32_e32 v162, v36, v37
	ds_read_b128 v[36:39], v150 offset:19712
	ds_read_b128 v[52:55], v150 offset:19968
	ds_read_b128 v[56:59], v150 offset:20224
	ds_read_b128 v[60:63], v150 offset:20480
	ds_read_b128 v[68:71], v150 offset:20992
	ds_read_b128 v[88:91], v150 offset:21248
	v_add_f32_dpp v80, v80, v80 row_mirror row_mask:0xf bank_mask:0xf bound_ctrl:1
	s_waitcnt lgkmcnt(11)
	v_pk_fma_f32 v[120:121], v[120:121], v[80:81], v[72:73] op_sel_hi:[1,0,1]
	v_pk_fma_f32 v[122:123], v[122:123], v[80:81], v[74:75] op_sel_hi:[1,0,1]
	s_waitcnt lgkmcnt(7)
	v_pk_mul_f32 v[64:65], v[64:65], v[120:121]
	v_pk_mul_f32 v[40:41], v[40:41], v[120:121]
	v_pk_fma_f32 v[64:65], v[66:67], v[122:123], v[64:65]
	s_waitcnt lgkmcnt(6)
; #define LAS __attribute__((address_space(3)))
; #define SCAN_RS(N_, SEL_, CTRL_) _Pragma("unroll") for (int i = 0; i < (N_); ++i) { const float keep = (SEL_) ? yp[2 * i + 1] : yp[2 * i], send = (SEL_) ? yp[2 * i] : yp[2 * i + 1]; \
;                         yp[i] = keep + __builtin_bit_cast(float, __builtin_amdgcn_update_dpp(0, __builtin_bit_cast(int, send), (CTRL_), 0xF, 0xF, false)); }
; __device__ __forceinline__ void p5_scan_block(Frame& F, int sb) {
;     ...
;             for (int s = 0; s < SC_T; ++s) {
;                 f32x4 nw = w5, nr = r5, nk = k5, na = a5, nb = b5; float nv = v5;
;                 if (s + 2 < SC_T) { nw = *(const LAS f32x4*)(p + (s + 2) * 384); nr = *(const LAS f32x4*)(p + (s + 2) * 384 + 64); nk = *(const LAS f32x4*)(p + (s + 2) * 384 + 128);
;                     na = *(const LAS f32x4*)(p + (s + 2) * 384 + 256); nb = *(const LAS f32x4*)(p + (s + 2) * 384 + 320); nv = pv[(s + 2) * 384]; }
;                 const f32x2 pa = Sa * a4.lo + Sb * a4.hi;
;                 float sa = pa.x + pa.y;
;                 const f32x2 ta = Sa * w4.lo + k4.lo * vv, tb = Sb * w4.hi + k4.hi * vv;
;                 sa = dpp_add16(sa);
;                 Sa = ta + b4.lo * sa; Sb = tb + b4.hi * sa;
;                 const f32x2 py = Sa * r4.lo + Sb * r4.hi;
;                 yp[s & 15] = py.x + py.y;
;                 if ((s & 15) == 15) {
;     ...
;                     SCAN_RS(8, b3, 0x128) SCAN_RS(4, b2, 0x141) SCAN_RS(2, b1, 0x1B) SCAN_RS(1, b0, 0xB1)
	v_pk_fma_f32 v[40:41], v[48:49], v[92:93], v[40:41] op_sel_hi:[1,0,1]
	v_add_f32_e32 v64, v64, v65
	v_pk_mul_f32 v[42:43], v[42:43], v[122:123]
	v_pk_mul_f32 v[72:73], v[78:79], v[122:123]
	v_add_f32_dpp v48, v64, v64 quad_perm:[1,0,3,2] row_mask:0xf bank_mask:0xf bound_ctrl:1
	v_pk_fma_f32 v[42:43], v[50:51], v[92:93], v[42:43] op_sel_hi:[1,0,1]
	v_pk_fma_f32 v[72:73], v[76:77], v[120:121], v[72:73]
	v_add_f32_dpp v48, v48, v48 quad_perm:[2,3,0,1] row_mask:0xf bank_mask:0xf bound_ctrl:1
	v_add_f32_e32 v163, v72, v73
	ds_read_b128 v[72:75], v150 offset:21504
	ds_read_b128 v[76:79], v150 offset:21760
	ds_read_b128 v[80:83], v150 offset:22016
	ds_read_b128 v[84:87], v150 offset:22528
	ds_read2st64_b32 v[152:153], v151 offset0:87 offset1:93
	v_add_f32_dpp v48, v48, v48 row_half_mirror row_mask:0xf bank_mask:0xf bound_ctrl:1
	s_nop 1
	v_add_f32_dpp v48, v48, v48 row_mirror row_mask:0xf bank_mask:0xf bound_ctrl:1
	s_waitcnt lgkmcnt(10)
	v_pk_fma_f32 v[124:125], v[36:37], v[48:49], v[40:41] op_sel_hi:[1,0,1]
	v_pk_fma_f32 v[126:127], v[38:39], v[48:49], v[42:43] op_sel_hi:[1,0,1]
	s_waitcnt lgkmcnt(6)
	v_pk_mul_f32 v[68:69], v[68:69], v[124:125]
	v_pk_mul_f32 v[52:53], v[52:53], v[124:125]
	v_pk_fma_f32 v[68:69], v[70:71], v[126:127], v[68:69]
	v_pk_mul_f32 v[54:55], v[54:55], v[126:127]
	v_add_f32_e32 v69, v68, v69
	v_mov_b32_e32 v68, v93
	v_pk_fma_f32 v[52:53], v[60:61], v[68:69], v[52:53] op_sel_hi:[1,0,1]
	v_add_f32_dpp v60, v69, v69 quad_perm:[1,0,3,2] row_mask:0xf bank_mask:0xf bound_ctrl:1
	v_pk_fma_f32 v[54:55], v[62:63], v[68:69], v[54:55] op_sel_hi:[1,0,1]
	v_pk_mul_f32 v[36:37], v[46:47], v[126:127]
	v_add_f32_dpp v60, v60, v60 quad_perm:[2,3,0,1] row_mask:0xf bank_mask:0xf bound_ctrl:1
	v_pk_fma_f32 v[36:37], v[44:45], v[124:125], v[36:37]
	s_nop 0
	v_add_f32_dpp v60, v60, v60 row_half_mirror row_mask:0xf bank_mask:0xf bound_ctrl:1
	v_add_f32_e32 v164, v36, v37
	ds_read_b128 v[36:39], v150 offset:22784
	ds_read_b128 v[40:43], v150 offset:23040
	ds_read_b128 v[44:47], v150 offset:23296
	ds_read_b128 v[48:51], v150 offset:23552
	ds_read_b128 v[64:67], v150 offset:24064
	ds_read_b128 v[120:123], v150 offset:24320
	v_add_f32_dpp v60, v60, v60 row_mirror row_mask:0xf bank_mask:0xf bound_ctrl:1
	s_waitcnt lgkmcnt(11)
	v_pk_fma_f32 v[88:89], v[88:89], v[60:61], v[52:53] op_sel_hi:[1,0,1]
	v_pk_fma_f32 v[90:91], v[90:91], v[60:61], v[54:55] op_sel_hi:[1,0,1]
	s_waitcnt lgkmcnt(7)
	v_pk_mul_f32 v[84:85], v[84:85], v[88:89]
	v_pk_mul_f32 v[72:73], v[72:73], v[88:89]
	v_pk_fma_f32 v[84:85], v[86:87], v[90:91], v[84:85]
	s_waitcnt lgkmcnt(6)
	v_pk_fma_f32 v[72:73], v[80:81], v[152:153], v[72:73] op_sel_hi:[1,0,1]
	v_add_f32_e32 v84, v84, v85
	v_pk_mul_f32 v[74:75], v[74:75], v[90:91]
	v_pk_mul_f32 v[52:53], v[58:59], v[90:91]
	v_add_f32_dpp v80, v84, v84 quad_perm:[1,0,3,2] row_mask:0xf bank_mask:0xf bound_ctrl:1
	v_pk_fma_f32 v[74:75], v[82:83], v[152:153], v[74:75] op_sel_hi:[1,0,1]
	v_pk_fma_f32 v[52:53], v[56:57], v[88:89], v[52:53]
	v_add_f32_dpp v80, v80, v80 quad_perm:[2,3,0,1] row_mask:0xf bank_mask:0xf bound_ctrl:1
	v_add_f32_e32 v165, v52, v53
	ds_read_b128 v[52:55], v150 offset:24576
	ds_read_b128 v[56:59], v150 offset:24832
	ds_read_b128 v[60:63], v150 offset:25088
	ds_read_b128 v[68:71], v150 offset:25600
	ds_read2st64_b32 v[92:93], v151 offset0:99 offset1:105
	v_add_f32_dpp v80, v80, v80 row_half_mirror row_mask:0xf bank_mask:0xf bound_ctrl:1
	s_nop 1
	v_add_f32_dpp v80, v80, v80 row_mirror row_mask:0xf bank_mask:0xf bound_ctrl:1
	s_waitcnt lgkmcnt(10)
	v_pk_fma_f32 v[36:37], v[36:37], v[80:81], v[72:73] op_sel_hi:[1,0,1]
	v_pk_fma_f32 v[38:39], v[38:39], v[80:81], v[74:75] op_sel_hi:[1,0,1]
	s_waitcnt lgkmcnt(6)
	v_pk_mul_f32 v[64:65], v[64:65], v[36:37]
	v_pk_mul_f32 v[72:73], v[78:79], v[38:39]
	v_pk_fma_f32 v[64:65], v[66:67], v[38:39], v[64:65]
	v_pk_fma_f32 v[72:73], v[76:77], v[36:37], v[72:73]
	v_add_f32_e32 v64, v64, v65
	v_pk_mul_f32 v[36:37], v[40:41], v[36:37]
	v_mov_b32_e32 v40, v153
	v_pk_mul_f32 v[38:39], v[42:43], v[38:39]
	v_pk_fma_f32 v[36:37], v[48:49], v[40:41], v[36:37] op_sel_hi:[1,0,1]
	v_pk_fma_f32 v[38:39], v[50:51], v[40:41], v[38:39] op_sel_hi:[1,0,1]
	v_add_f32_dpp v40, v64, v64 quad_perm:[1,0,3,2] row_mask:0xf bank_mask:0xf bound_ctrl:1
	v_add_f32_e32 v152, v72, v73
	v_cndmask_b32_e64 v42, v164, v165, s[8:9]
	v_add_f32_dpp v40, v40, v40 quad_perm:[2,3,0,1] row_mask:0xf bank_mask:0xf bound_ctrl:1
	ds_read_b128 v[72:75], v150 offset:25856
	ds_read_b128 v[76:79], v150 offset:26112
	ds_read_b128 v[80:83], v150 offset:26368
	ds_read_b128 v[84:87], v150 offset:26624
	ds_read_b128 v[88:91], v150 offset:27136
	ds_read_b128 v[124:127], v150 offset:27392
	v_add_f32_dpp v40, v40, v40 row_half_mirror row_mask:0xf bank_mask:0xf bound_ctrl:1
	s_nop 1
	v_add_f32_dpp v40, v40, v40 row_mirror row_mask:0xf bank_mask:0xf bound_ctrl:1
	s_waitcnt lgkmcnt(11)
	v_pk_fma_f32 v[64:65], v[122:123], v[40:41], v[38:39] op_sel_hi:[1,0,1]
	v_pk_fma_f32 v[50:51], v[120:121], v[40:41], v[36:37] op_sel_hi:[1,0,1]
	v_pk_mul_f32 v[36:37], v[46:47], v[64:65]
	v_cndmask_b32_e64 v38, v156, v157, s[8:9]
	v_pk_fma_f32 v[36:37], v[44:45], v[50:51], v[36:37]
	v_cndmask_b32_e64 v39, v158, v159, s[8:9]
	v_add_f32_e32 v36, v36, v37
	v_cndmask_b32_e64 v37, v35, v34, s[8:9]
	v_cndmask_b32_e64 v34, v34, v35, s[8:9]
	v_cndmask_b32_e64 v35, v155, v154, s[8:9]
	v_cndmask_b32_e64 v40, v160, v161, s[8:9]
	v_add_f32_dpp v34, v34, v37 row_ror:8 row_mask:0xf bank_mask:0xf bound_ctrl:1
	v_cndmask_b32_e64 v37, v154, v155, s[8:9]
	s_waitcnt lgkmcnt(7)
; #define LAS __attribute__((address_space(3)))
; #define SCAN_RS(N_, SEL_, CTRL_) _Pragma("unroll") for (int i = 0; i < (N_); ++i) { const float keep = (SEL_) ? yp[2 * i + 1] : yp[2 * i], send = (SEL_) ? yp[2 * i] : yp[2 * i + 1]; \
;                         yp[i] = keep + __builtin_bit_cast(float, __builtin_amdgcn_update_dpp(0, __builtin_bit_cast(int, send), (CTRL_), 0xF, 0xF, false)); }
; __device__ __forceinline__ void p5_scan_block(Frame& F, int sb) {
;     ...
;             for (int s = 0; s < SC_T; ++s) {
;                 f32x4 nw = w5, nr = r5, nk = k5, na = a5, nb = b5; float nv = v5;
;                 if (s + 2 < SC_T) { nw = *(const LAS f32x4*)(p + (s + 2) * 384); nr = *(const LAS f32x4*)(p + (s + 2) * 384 + 64); nk = *(const LAS f32x4*)(p + (s + 2) * 384 + 128);
;                     na = *(const LAS f32x4*)(p + (s + 2) * 384 + 256); nb = *(const LAS f32x4*)(p + (s + 2) * 384 + 320); nv = pv[(s + 2) * 384]; }
;                 const f32x2 pa = Sa * a4.lo + Sb * a4.hi;
;                 float sa = pa.x + pa.y;
;                 const f32x2 ta = Sa * w4.lo + k4.lo * vv, tb = Sb * w4.hi + k4.hi * vv;
;                 sa = dpp_add16(sa);
;                 Sa = ta + b4.lo * sa; Sb = tb + b4.hi * sa;
;                 const f32x2 py = Sa * r4.lo + Sb * r4.hi;
;                 yp[s & 15] = py.x + py.y;
;                 if ((s & 15) == 15) {
;     ...
;                     SCAN_RS(8, b3, 0x128) SCAN_RS(4, b2, 0x141) SCAN_RS(2, b1, 0x1B) SCAN_RS(1, b0, 0xB1)
;     ...
;                     yo[((s & 16) + qidx) * 16] = yp[0];
;                 }
	v_pk_mul_f32 v[66:67], v[68:69], v[50:51]
	v_cndmask_b32_e64 v41, v162, v163, s[8:9]
	v_add_f32_dpp v35, v37, v35 row_ror:8 row_mask:0xf bank_mask:0xf bound_ctrl:1
	v_cndmask_b32_e64 v37, v157, v156, s[8:9]
	v_pk_fma_f32 v[66:67], v[70:71], v[64:65], v[66:67]
	v_pk_mul_f32 v[50:51], v[52:53], v[50:51]
	v_add_f32_dpp v37, v38, v37 row_ror:8 row_mask:0xf bank_mask:0xf bound_ctrl:1
	v_cndmask_b32_e64 v38, v159, v158, s[8:9]
	v_add_f32_e32 v66, v66, v67
	v_pk_mul_f32 v[52:53], v[54:55], v[64:65]
	v_add_f32_dpp v38, v39, v38 row_ror:8 row_mask:0xf bank_mask:0xf bound_ctrl:1
	v_cndmask_b32_e64 v39, v161, v160, s[8:9]
	v_add_f32_dpp v54, v66, v66 quad_perm:[1,0,3,2] row_mask:0xf bank_mask:0xf bound_ctrl:1
	s_waitcnt lgkmcnt(6)
	v_pk_fma_f32 v[50:51], v[60:61], v[92:93], v[50:51] op_sel_hi:[1,0,1]
	v_add_f32_dpp v39, v40, v39 row_ror:8 row_mask:0xf bank_mask:0xf bound_ctrl:1
	v_cndmask_b32_e64 v40, v163, v162, s[8:9]
	v_add_f32_dpp v54, v54, v54 quad_perm:[2,3,0,1] row_mask:0xf bank_mask:0xf bound_ctrl:1
	v_pk_fma_f32 v[52:53], v[62:63], v[92:93], v[52:53] op_sel_hi:[1,0,1]
	v_add_f32_dpp v40, v41, v40 row_ror:8 row_mask:0xf bank_mask:0xf bound_ctrl:1
	v_cndmask_b32_e64 v41, v165, v164, s[8:9]
	v_add_f32_dpp v54, v54, v54 row_half_mirror row_mask:0xf bank_mask:0xf bound_ctrl:1
	s_nop 0
	v_add_f32_dpp v41, v42, v41 row_ror:8 row_mask:0xf bank_mask:0xf bound_ctrl:1
	v_cndmask_b32_e64 v42, v36, v152, s[8:9]
	v_cndmask_b32_e64 v36, v152, v36, s[8:9]
	v_add_f32_dpp v54, v54, v54 row_mirror row_mask:0xf bank_mask:0xf bound_ctrl:1
	s_waitcnt lgkmcnt(5)
	v_pk_fma_f32 v[62:63], v[72:73], v[54:55], v[50:51] op_sel_hi:[1,0,1]
	v_add_f32_dpp v36, v36, v42 row_ror:8 row_mask:0xf bank_mask:0xf bound_ctrl:1
	v_cndmask_b32_e64 v42, v35, v34, s[6:7]
	v_cndmask_b32_e64 v34, v34, v35, s[6:7]
	v_cndmask_b32_e64 v35, v38, v37, s[6:7]
	v_cndmask_b32_e64 v37, v37, v38, s[6:7]
	v_cndmask_b32_e64 v38, v39, v40, s[6:7]
	v_add_f32_dpp v34, v34, v42 row_half_mirror row_mask:0xf bank_mask:0xf bound_ctrl:1
	v_add_f32_dpp v35, v37, v35 row_half_mirror row_mask:0xf bank_mask:0xf bound_ctrl:1
	v_cndmask_b32_e64 v37, v40, v39, s[6:7]
	v_pk_fma_f32 v[64:65], v[74:75], v[54:55], v[52:53] op_sel_hi:[1,0,1]
	s_waitcnt lgkmcnt(1)
	v_pk_mul_f32 v[70:71], v[88:89], v[62:63]
	v_add_f32_dpp v37, v38, v37 row_half_mirror row_mask:0xf bank_mask:0xf bound_ctrl:1
	v_cndmask_b32_e64 v38, v36, v41, s[6:7]
	v_cndmask_b32_e64 v36, v41, v36, s[6:7]
	v_pk_mul_f32 v[50:51], v[58:59], v[64:65]
	v_pk_fma_f32 v[70:71], v[90:91], v[64:65], v[70:71]
	v_add_f32_dpp v36, v36, v38 row_half_mirror row_mask:0xf bank_mask:0xf bound_ctrl:1
	v_cndmask_b32_e64 v38, v35, v34, s[4:5]
	v_cndmask_b32_e64 v34, v34, v35, s[4:5]
	v_cndmask_b32_e64 v35, v36, v37, s[4:5]
	v_cndmask_b32_e64 v36, v37, v36, s[4:5]
	v_add_f32_dpp v34, v34, v38 quad_perm:[3,2,1,0] row_mask:0xf bank_mask:0xf bound_ctrl:1
	v_pk_fma_f32 v[50:51], v[56:57], v[62:63], v[50:51]
	v_add_f32_dpp v35, v36, v35 quad_perm:[3,2,1,0] row_mask:0xf bank_mask:0xf bound_ctrl:1
	v_cndmask_b32_e64 v36, v35, v34, s[0:1]
	v_cndmask_b32_e64 v34, v34, v35, s[0:1]
	v_add_f32_e32 v71, v70, v71
	v_pk_mul_f32 v[62:63], v[76:77], v[62:63]
	v_mov_b32_e32 v70, v93
	v_pk_mul_f32 v[64:65], v[78:79], v[64:65]
	v_add_f32_dpp v34, v34, v36 quad_perm:[1,0,3,2] row_mask:0xf bank_mask:0xf bound_ctrl:1
	v_lshl_add_u32 v152, s44, 11, v149
	v_pk_fma_f32 v[62:63], v[84:85], v[70:71], v[62:63] op_sel_hi:[1,0,1]
	v_pk_fma_f32 v[64:65], v[86:87], v[70:71], v[64:65] op_sel_hi:[1,0,1]
	v_add_f32_dpp v70, v71, v71 quad_perm:[1,0,3,2] row_mask:0xf bank_mask:0xf bound_ctrl:1
	ds_write_b32 v152, v34
	ds_read_b128 v[42:45], v150 offset:27648
	ds_read_b128 v[34:37], v150 offset:27904
	ds_read_b128 v[46:49], v150 offset:28160
	ds_read_b128 v[156:159], v150 offset:28672
	ds_read_b128 v[38:41], v150 offset:28928
	ds_read2st64_b32 v[120:121], v151 offset0:111 offset1:117
	v_add_f32_dpp v70, v70, v70 quad_perm:[2,3,0,1] row_mask:0xf bank_mask:0xf bound_ctrl:1
	v_add_f32_e32 v153, v50, v51
	ds_read_b128 v[54:57], v150 offset:29184
	ds_read_b128 v[50:53], v150 offset:29440
	ds_read_b128 v[58:61], v150 offset:29696
	ds_read_b128 v[66:69], v150 offset:30208
	v_add_f32_dpp v70, v70, v70 row_half_mirror row_mask:0xf bank_mask:0xf bound_ctrl:1
	s_nop 1
	v_add_f32_dpp v70, v70, v70 row_mirror row_mask:0xf bank_mask:0xf bound_ctrl:1
	s_waitcnt lgkmcnt(11)
	v_pk_fma_f32 v[124:125], v[124:125], v[70:71], v[62:63] op_sel_hi:[1,0,1]
	v_pk_fma_f32 v[126:127], v[126:127], v[70:71], v[64:65] op_sel_hi:[1,0,1]
	s_waitcnt lgkmcnt(6)
	v_pk_mul_f32 v[90:91], v[156:157], v[124:125]
	v_pk_mul_f32 v[42:43], v[42:43], v[124:125]
	v_pk_fma_f32 v[90:91], v[158:159], v[126:127], v[90:91]
	s_waitcnt lgkmcnt(4)
	v_pk_fma_f32 v[42:43], v[46:47], v[120:121], v[42:43] op_sel_hi:[1,0,1]
	v_add_f32_e32 v155, v90, v91
	v_pk_mul_f32 v[62:63], v[82:83], v[126:127]
	v_pk_mul_f32 v[44:45], v[44:45], v[126:127]
	v_add_f32_dpp v46, v155, v155 quad_perm:[1,0,3,2] row_mask:0xf bank_mask:0xf bound_ctrl:1
	v_pk_fma_f32 v[62:63], v[80:81], v[124:125], v[62:63]
	v_pk_fma_f32 v[44:45], v[48:49], v[120:121], v[44:45] op_sel_hi:[1,0,1]
	v_add_f32_dpp v46, v46, v46 quad_perm:[2,3,0,1] row_mask:0xf bank_mask:0xf bound_ctrl:1
	v_add_f32_e32 v154, v62, v63
	ds_read_b128 v[86:89], v150 offset:30464
	ds_read_b128 v[74:77], v150 offset:30720
	ds_read_b128 v[62:65], v150 offset:30976
	ds_read_b128 v[78:81], v150 offset:31232
	ds_read_b128 v[82:85], v150 offset:31744
	ds_read_b128 v[70:73], v150 offset:32000
	ds_read2st64_b32 v[122:123], v151 offset0:123 offset1:129
	v_add_f32_dpp v46, v46, v46 row_half_mirror row_mask:0xf bank_mask:0xf bound_ctrl:1
	ds_read_b128 v[90:93], v150 offset:48896
	s_nop 0
	v_add_f32_dpp v46, v46, v46 row_mirror row_mask:0xf bank_mask:0xf bound_ctrl:1
	v_pk_fma_f32 v[124:125], v[38:39], v[46:47], v[42:43] op_sel_hi:[1,0,1]
	v_pk_fma_f32 v[126:127], v[40:41], v[46:47], v[44:45] op_sel_hi:[1,0,1]
	s_waitcnt lgkmcnt(8)
; #define LAS __attribute__((address_space(3)))
; __device__ __forceinline__ void p5_scan_block(Frame& F, int sb) {
;     ...
;             for (int s = 0; s < SC_T; ++s) {
;                 f32x4 nw = w5, nr = r5, nk = k5, na = a5, nb = b5; float nv = v5;
;                 if (s + 2 < SC_T) { nw = *(const LAS f32x4*)(p + (s + 2) * 384); nr = *(const LAS f32x4*)(p + (s + 2) * 384 + 64); nk = *(const LAS f32x4*)(p + (s + 2) * 384 + 128);
;                     na = *(const LAS f32x4*)(p + (s + 2) * 384 + 256); nb = *(const LAS f32x4*)(p + (s + 2) * 384 + 320); nv = pv[(s + 2) * 384]; }
;                 const f32x2 pa = Sa * a4.lo + Sb * a4.hi;
;                 float sa = pa.x + pa.y;
;                 const f32x2 ta = Sa * w4.lo + k4.lo * vv, tb = Sb * w4.hi + k4.hi * vv;
;                 sa = dpp_add16(sa);
;                 Sa = ta + b4.lo * sa; Sb = tb + b4.hi * sa;
;                 const f32x2 py = Sa * r4.lo + Sb * r4.hi;
;                 yp[s & 15] = py.x + py.y;
	v_pk_mul_f32 v[66:67], v[66:67], v[124:125]
	v_pk_mul_f32 v[54:55], v[54:55], v[124:125]
	v_pk_fma_f32 v[66:67], v[68:69], v[126:127], v[66:67]
	v_pk_mul_f32 v[56:57], v[56:57], v[126:127]
	v_add_f32_e32 v67, v66, v67
	v_mov_b32_e32 v66, v121
	v_pk_fma_f32 v[54:55], v[58:59], v[66:67], v[54:55] op_sel_hi:[1,0,1]
	v_add_f32_dpp v58, v67, v67 quad_perm:[1,0,3,2] row_mask:0xf bank_mask:0xf bound_ctrl:1
	v_pk_fma_f32 v[56:57], v[60:61], v[66:67], v[56:57] op_sel_hi:[1,0,1]
	v_pk_mul_f32 v[36:37], v[36:37], v[126:127]
	v_add_f32_dpp v58, v58, v58 quad_perm:[2,3,0,1] row_mask:0xf bank_mask:0xf bound_ctrl:1
	v_pk_fma_f32 v[34:35], v[34:35], v[124:125], v[36:37]
	s_nop 0
	v_add_f32_dpp v58, v58, v58 row_half_mirror row_mask:0xf bank_mask:0xf bound_ctrl:1
	v_add_f32_e32 v155, v34, v35
	ds_read_b128 v[34:37], v150 offset:32256
	ds_read_b128 v[38:41], v150 offset:32512
	ds_read_b128 v[42:45], v150 offset:32768
	ds_read_b128 v[46:49], v150 offset:33280
	v_add_f32_dpp v58, v58, v58 row_mirror row_mask:0xf bank_mask:0xf bound_ctrl:1
	s_waitcnt lgkmcnt(11)
	v_pk_fma_f32 v[120:121], v[86:87], v[58:59], v[54:55] op_sel_hi:[1,0,1]
	v_pk_fma_f32 v[156:157], v[88:89], v[58:59], v[56:57] op_sel_hi:[1,0,1]
	s_waitcnt lgkmcnt(7)
	v_pk_mul_f32 v[82:83], v[82:83], v[120:121]
	v_pk_mul_f32 v[74:75], v[74:75], v[120:121]
	v_pk_fma_f32 v[82:83], v[84:85], v[156:157], v[82:83]
	s_waitcnt lgkmcnt(5)
	v_pk_fma_f32 v[74:75], v[78:79], v[122:123], v[74:75] op_sel_hi:[1,0,1]
	v_add_f32_e32 v82, v82, v83
	v_pk_mul_f32 v[76:77], v[76:77], v[156:157]
	v_pk_mul_f32 v[52:53], v[52:53], v[156:157]
	v_add_f32_dpp v78, v82, v82 quad_perm:[1,0,3,2] row_mask:0xf bank_mask:0xf bound_ctrl:1
	v_pk_fma_f32 v[76:77], v[80:81], v[122:123], v[76:77] op_sel_hi:[1,0,1]
	v_pk_fma_f32 v[50:51], v[50:51], v[120:121], v[52:53]
	v_add_f32_dpp v78, v78, v78 quad_perm:[2,3,0,1] row_mask:0xf bank_mask:0xf bound_ctrl:1
	v_add_f32_e32 v160, v50, v51
	ds_read_b128 v[50:53], v150 offset:33536
	ds_read_b128 v[54:57], v150 offset:33792
	ds_read_b128 v[58:61], v150 offset:34048
	ds_read_b128 v[66:69], v150 offset:34304
	ds_read_b128 v[86:89], v150 offset:34816
	ds_read_b128 v[124:127], v150 offset:35072
	ds_read2st64_b32 v[158:159], v151 offset0:135 offset1:141
	v_add_f32_dpp v78, v78, v78 row_half_mirror row_mask:0xf bank_mask:0xf bound_ctrl:1
	s_nop 1
	v_add_f32_dpp v78, v78, v78 row_mirror row_mask:0xf bank_mask:0xf bound_ctrl:1
	v_pk_fma_f32 v[82:83], v[70:71], v[78:79], v[74:75] op_sel_hi:[1,0,1]
	v_pk_fma_f32 v[84:85], v[72:73], v[78:79], v[76:77] op_sel_hi:[1,0,1]
	s_waitcnt lgkmcnt(7)
	v_pk_mul_f32 v[46:47], v[46:47], v[82:83]
	v_pk_mul_f32 v[34:35], v[34:35], v[82:83]
	v_pk_fma_f32 v[46:47], v[48:49], v[84:85], v[46:47]
	v_pk_mul_f32 v[36:37], v[36:37], v[84:85]
	v_add_f32_e32 v47, v46, v47
	v_mov_b32_e32 v46, v123
	v_pk_fma_f32 v[34:35], v[42:43], v[46:47], v[34:35] op_sel_hi:[1,0,1]
	v_add_f32_dpp v42, v47, v47 quad_perm:[1,0,3,2] row_mask:0xf bank_mask:0xf bound_ctrl:1
	v_pk_fma_f32 v[36:37], v[44:45], v[46:47], v[36:37] op_sel_hi:[1,0,1]
	v_pk_mul_f32 v[64:65], v[64:65], v[84:85]
	v_add_f32_dpp v42, v42, v42 quad_perm:[2,3,0,1] row_mask:0xf bank_mask:0xf bound_ctrl:1
	v_pk_fma_f32 v[62:63], v[62:63], v[82:83], v[64:65]
	s_nop 0
	v_add_f32_dpp v42, v42, v42 row_half_mirror row_mask:0xf bank_mask:0xf bound_ctrl:1
	v_add_f32_e32 v161, v62, v63
	ds_read_b128 v[62:65], v150 offset:35328
	ds_read_b128 v[70:73], v150 offset:35584
	ds_read_b128 v[74:77], v150 offset:35840
	ds_read_b128 v[78:81], v150 offset:36352
	v_add_f32_dpp v42, v42, v42 row_mirror row_mask:0xf bank_mask:0xf bound_ctrl:1
	s_waitcnt lgkmcnt(10)
	v_pk_fma_f32 v[120:121], v[50:51], v[42:43], v[34:35] op_sel_hi:[1,0,1]
	v_pk_fma_f32 v[122:123], v[52:53], v[42:43], v[36:37] op_sel_hi:[1,0,1]
	s_waitcnt lgkmcnt(6)
	v_pk_mul_f32 v[86:87], v[86:87], v[120:121]
	v_pk_mul_f32 v[54:55], v[54:55], v[120:121]
	v_pk_fma_f32 v[86:87], v[88:89], v[122:123], v[86:87]
	s_waitcnt lgkmcnt(4)
	v_pk_fma_f32 v[54:55], v[66:67], v[158:159], v[54:55] op_sel_hi:[1,0,1]
	v_add_f32_e32 v86, v86, v87
	v_pk_mul_f32 v[34:35], v[40:41], v[122:123]
	v_pk_mul_f32 v[56:57], v[56:57], v[122:123]
	v_add_f32_dpp v66, v86, v86 quad_perm:[1,0,3,2] row_mask:0xf bank_mask:0xf bound_ctrl:1
	v_pk_fma_f32 v[34:35], v[38:39], v[120:121], v[34:35]
	v_pk_fma_f32 v[56:57], v[68:69], v[158:159], v[56:57] op_sel_hi:[1,0,1]
	v_add_f32_dpp v66, v66, v66 quad_perm:[2,3,0,1] row_mask:0xf bank_mask:0xf bound_ctrl:1
	v_add_f32_e32 v162, v34, v35
	ds_read_b128 v[34:37], v150 offset:36608
	ds_read_b128 v[38:41], v150 offset:36864
	ds_read_b128 v[42:45], v150 offset:37120
	ds_read_b128 v[46:49], v150 offset:37376
	ds_read_b128 v[50:53], v150 offset:37888
	ds_read_b128 v[82:85], v150 offset:38144
	ds_read2st64_b32 v[156:157], v151 offset0:147 offset1:153
	v_add_f32_dpp v66, v66, v66 row_half_mirror row_mask:0xf bank_mask:0xf bound_ctrl:1
	s_nop 1
	v_add_f32_dpp v66, v66, v66 row_mirror row_mask:0xf bank_mask:0xf bound_ctrl:1
	v_pk_fma_f32 v[120:121], v[124:125], v[66:67], v[54:55] op_sel_hi:[1,0,1]
	v_pk_fma_f32 v[122:123], v[126:127], v[66:67], v[56:57] op_sel_hi:[1,0,1]
	s_waitcnt lgkmcnt(7)
; #define LAS __attribute__((address_space(3)))
; __device__ __forceinline__ void p5_scan_block(Frame& F, int sb) {
;     ...
;             for (int s = 0; s < SC_T; ++s) {
;                 f32x4 nw = w5, nr = r5, nk = k5, na = a5, nb = b5; float nv = v5;
;                 if (s + 2 < SC_T) { nw = *(const LAS f32x4*)(p + (s + 2) * 384); nr = *(const LAS f32x4*)(p + (s + 2) * 384 + 64); nk = *(const LAS f32x4*)(p + (s + 2) * 384 + 128);
;                     na = *(const LAS f32x4*)(p + (s + 2) * 384 + 256); nb = *(const LAS f32x4*)(p + (s + 2) * 384 + 320); nv = pv[(s + 2) * 384]; }
;                 const f32x2 pa = Sa * a4.lo + Sb * a4.hi;
;                 float sa = pa.x + pa.y;
;                 const f32x2 ta = Sa * w4.lo + k4.lo * vv, tb = Sb * w4.hi + k4.hi * vv;
;                 sa = dpp_add16(sa);
;                 Sa = ta + b4.lo * sa; Sb = tb + b4.hi * sa;
;                 const f32x2 py = Sa * r4.lo + Sb * r4.hi;
;                 yp[s & 15] = py.x + py.y;
	v_pk_mul_f32 v[78:79], v[78:79], v[120:121]
	v_pk_mul_f32 v[62:63], v[62:63], v[120:121]
	v_pk_fma_f32 v[78:79], v[80:81], v[122:123], v[78:79]
	v_pk_mul_f32 v[64:65], v[64:65], v[122:123]
	v_add_f32_e32 v79, v78, v79
	v_mov_b32_e32 v78, v159
	v_pk_fma_f32 v[62:63], v[74:75], v[78:79], v[62:63] op_sel_hi:[1,0,1]
	v_add_f32_dpp v74, v79, v79 quad_perm:[1,0,3,2] row_mask:0xf bank_mask:0xf bound_ctrl:1
	v_pk_fma_f32 v[64:65], v[76:77], v[78:79], v[64:65] op_sel_hi:[1,0,1]
	v_pk_mul_f32 v[54:55], v[60:61], v[122:123]
	v_add_f32_dpp v74, v74, v74 quad_perm:[2,3,0,1] row_mask:0xf bank_mask:0xf bound_ctrl:1
	v_pk_fma_f32 v[54:55], v[58:59], v[120:121], v[54:55]
	s_nop 0
	v_add_f32_dpp v74, v74, v74 row_half_mirror row_mask:0xf bank_mask:0xf bound_ctrl:1
	v_add_f32_e32 v163, v54, v55
	ds_read_b128 v[54:57], v150 offset:38400
	ds_read_b128 v[58:61], v150 offset:38656
	ds_read_b128 v[66:69], v150 offset:38912
	ds_read_b128 v[86:89], v150 offset:39424
	v_add_f32_dpp v74, v74, v74 row_mirror row_mask:0xf bank_mask:0xf bound_ctrl:1
	s_waitcnt lgkmcnt(10)
	v_pk_fma_f32 v[124:125], v[34:35], v[74:75], v[62:63] op_sel_hi:[1,0,1]
	v_pk_fma_f32 v[126:127], v[36:37], v[74:75], v[64:65] op_sel_hi:[1,0,1]
	s_waitcnt lgkmcnt(6)
	v_pk_mul_f32 v[50:51], v[50:51], v[124:125]
	v_pk_mul_f32 v[38:39], v[38:39], v[124:125]
	v_pk_fma_f32 v[50:51], v[52:53], v[126:127], v[50:51]
	s_waitcnt lgkmcnt(4)
	v_pk_fma_f32 v[38:39], v[46:47], v[156:157], v[38:39] op_sel_hi:[1,0,1]
	v_add_f32_e32 v50, v50, v51
	v_pk_mul_f32 v[40:41], v[40:41], v[126:127]
	v_pk_mul_f32 v[34:35], v[72:73], v[126:127]
	v_add_f32_dpp v46, v50, v50 quad_perm:[1,0,3,2] row_mask:0xf bank_mask:0xf bound_ctrl:1
	v_pk_fma_f32 v[40:41], v[48:49], v[156:157], v[40:41] op_sel_hi:[1,0,1]
	v_pk_fma_f32 v[34:35], v[70:71], v[124:125], v[34:35]
	v_add_f32_dpp v46, v46, v46 quad_perm:[2,3,0,1] row_mask:0xf bank_mask:0xf bound_ctrl:1
	v_add_f32_e32 v164, v34, v35
	ds_read_b128 v[34:37], v150 offset:39680
	ds_read_b128 v[62:65], v150 offset:39936
	ds_read_b128 v[70:73], v150 offset:40192
	ds_read_b128 v[74:77], v150 offset:40448
	ds_read_b128 v[78:81], v150 offset:40960
	ds_read_b128 v[120:123], v150 offset:41216
	ds_read2st64_b32 v[158:159], v151 offset0:159 offset1:165
	v_add_f32_dpp v46, v46, v46 row_half_mirror row_mask:0xf bank_mask:0xf bound_ctrl:1
	s_nop 1
	v_add_f32_dpp v46, v46, v46 row_mirror row_mask:0xf bank_mask:0xf bound_ctrl:1
	v_pk_fma_f32 v[82:83], v[82:83], v[46:47], v[38:39] op_sel_hi:[1,0,1]
	v_pk_fma_f32 v[84:85], v[84:85], v[46:47], v[40:41] op_sel_hi:[1,0,1]
	s_waitcnt lgkmcnt(7)
	v_pk_mul_f32 v[86:87], v[86:87], v[82:83]
	v_pk_mul_f32 v[38:39], v[44:45], v[84:85]
	v_pk_fma_f32 v[86:87], v[88:89], v[84:85], v[86:87]
	v_pk_fma_f32 v[38:39], v[42:43], v[82:83], v[38:39]
	v_add_f32_e32 v86, v86, v87
	v_pk_mul_f32 v[54:55], v[54:55], v[82:83]
	v_mov_b32_e32 v82, v157
	v_pk_fma_f32 v[54:55], v[66:67], v[82:83], v[54:55] op_sel_hi:[1,0,1]
	v_add_f32_dpp v66, v86, v86 quad_perm:[1,0,3,2] row_mask:0xf bank_mask:0xf bound_ctrl:1
	v_pk_mul_f32 v[56:57], v[56:57], v[84:85]
	v_add_f32_e32 v165, v38, v39
	v_add_f32_dpp v66, v66, v66 quad_perm:[2,3,0,1] row_mask:0xf bank_mask:0xf bound_ctrl:1
	v_pk_fma_f32 v[56:57], v[68:69], v[82:83], v[56:57] op_sel_hi:[1,0,1]
	ds_read_b128 v[38:41], v150 offset:41472
	ds_read_b128 v[42:45], v150 offset:41728
	ds_read_b128 v[46:49], v150 offset:41984
	ds_read_b128 v[50:53], v150 offset:42496
	v_add_f32_dpp v66, v66, v66 row_half_mirror row_mask:0xf bank_mask:0xf bound_ctrl:1
	s_nop 1
	v_add_f32_dpp v66, v66, v66 row_mirror row_mask:0xf bank_mask:0xf bound_ctrl:1
	s_waitcnt lgkmcnt(10)
	v_pk_fma_f32 v[124:125], v[34:35], v[66:67], v[54:55] op_sel_hi:[1,0,1]
	v_pk_fma_f32 v[126:127], v[36:37], v[66:67], v[56:57] op_sel_hi:[1,0,1]
	s_waitcnt lgkmcnt(6)
	v_pk_mul_f32 v[78:79], v[78:79], v[124:125]
	v_pk_mul_f32 v[62:63], v[62:63], v[124:125]
	v_pk_fma_f32 v[78:79], v[80:81], v[126:127], v[78:79]
	s_waitcnt lgkmcnt(4)
	v_pk_fma_f32 v[62:63], v[74:75], v[158:159], v[62:63] op_sel_hi:[1,0,1]
	v_add_f32_e32 v78, v78, v79
	v_pk_mul_f32 v[64:65], v[64:65], v[126:127]
	v_pk_mul_f32 v[34:35], v[60:61], v[126:127]
	v_add_f32_dpp v74, v78, v78 quad_perm:[1,0,3,2] row_mask:0xf bank_mask:0xf bound_ctrl:1
	v_pk_fma_f32 v[64:65], v[76:77], v[158:159], v[64:65] op_sel_hi:[1,0,1]
	v_pk_fma_f32 v[34:35], v[58:59], v[124:125], v[34:35]
	v_add_f32_dpp v74, v74, v74 quad_perm:[2,3,0,1] row_mask:0xf bank_mask:0xf bound_ctrl:1
	v_add_f32_e32 v166, v34, v35
	ds_read_b128 v[34:37], v150 offset:42752
	ds_read_b128 v[54:57], v150 offset:43008
	ds_read_b128 v[58:61], v150 offset:43264
	ds_read_b128 v[66:69], v150 offset:43520
	ds_read_b128 v[82:85], v150 offset:44032
	ds_read_b128 v[86:89], v150 offset:44288
	ds_read2st64_b32 v[156:157], v151 offset0:171 offset1:177
	v_add_f32_dpp v74, v74, v74 row_half_mirror row_mask:0xf bank_mask:0xf bound_ctrl:1
	s_nop 1
	v_add_f32_dpp v74, v74, v74 row_mirror row_mask:0xf bank_mask:0xf bound_ctrl:1
	v_pk_fma_f32 v[120:121], v[120:121], v[74:75], v[62:63] op_sel_hi:[1,0,1]
	v_pk_fma_f32 v[122:123], v[122:123], v[74:75], v[64:65] op_sel_hi:[1,0,1]
	s_waitcnt lgkmcnt(7)
; #define LAS __attribute__((address_space(3)))
; __device__ __forceinline__ void p5_scan_block(Frame& F, int sb) {
;     ...
;             for (int s = 0; s < SC_T; ++s) {
;                 f32x4 nw = w5, nr = r5, nk = k5, na = a5, nb = b5; float nv = v5;
;                 if (s + 2 < SC_T) { nw = *(const LAS f32x4*)(p + (s + 2) * 384); nr = *(const LAS f32x4*)(p + (s + 2) * 384 + 64); nk = *(const LAS f32x4*)(p + (s + 2) * 384 + 128);
;                     na = *(const LAS f32x4*)(p + (s + 2) * 384 + 256); nb = *(const LAS f32x4*)(p + (s + 2) * 384 + 320); nv = pv[(s + 2) * 384]; }
;                 const f32x2 pa = Sa * a4.lo + Sb * a4.hi;
;                 float sa = pa.x + pa.y;
;                 const f32x2 ta = Sa * w4.lo + k4.lo * vv, tb = Sb * w4.hi + k4.hi * vv;
;                 sa = dpp_add16(sa);
;                 Sa = ta + b4.lo * sa; Sb = tb + b4.hi * sa;
;                 const f32x2 py = Sa * r4.lo + Sb * r4.hi;
;                 yp[s & 15] = py.x + py.y;
	v_pk_mul_f32 v[50:51], v[50:51], v[120:121]
	v_pk_mul_f32 v[38:39], v[38:39], v[120:121]
	v_pk_fma_f32 v[50:51], v[52:53], v[122:123], v[50:51]
	v_pk_mul_f32 v[40:41], v[40:41], v[122:123]
	v_add_f32_e32 v51, v50, v51
	v_mov_b32_e32 v50, v159
	v_pk_fma_f32 v[38:39], v[46:47], v[50:51], v[38:39] op_sel_hi:[1,0,1]
	v_add_f32_dpp v46, v51, v51 quad_perm:[1,0,3,2] row_mask:0xf bank_mask:0xf bound_ctrl:1
	v_pk_fma_f32 v[40:41], v[48:49], v[50:51], v[40:41] op_sel_hi:[1,0,1]
	v_pk_mul_f32 v[62:63], v[72:73], v[122:123]
	v_add_f32_dpp v46, v46, v46 quad_perm:[2,3,0,1] row_mask:0xf bank_mask:0xf bound_ctrl:1
	v_pk_fma_f32 v[62:63], v[70:71], v[120:121], v[62:63]
	s_nop 0
	v_add_f32_dpp v46, v46, v46 row_half_mirror row_mask:0xf bank_mask:0xf bound_ctrl:1
	v_add_f32_e32 v167, v62, v63
	ds_read_b128 v[62:65], v150 offset:44544
	ds_read_b128 v[70:73], v150 offset:44800
	ds_read_b128 v[74:77], v150 offset:45056
	ds_read_b128 v[78:81], v150 offset:45568
	v_add_f32_dpp v46, v46, v46 row_mirror row_mask:0xf bank_mask:0xf bound_ctrl:1
	s_waitcnt lgkmcnt(10)
	v_pk_fma_f32 v[124:125], v[34:35], v[46:47], v[38:39] op_sel_hi:[1,0,1]
	v_pk_fma_f32 v[126:127], v[36:37], v[46:47], v[40:41] op_sel_hi:[1,0,1]
	s_waitcnt lgkmcnt(6)
	v_pk_mul_f32 v[82:83], v[82:83], v[124:125]
	v_pk_mul_f32 v[54:55], v[54:55], v[124:125]
	v_pk_fma_f32 v[82:83], v[84:85], v[126:127], v[82:83]
	s_waitcnt lgkmcnt(4)
	v_pk_fma_f32 v[54:55], v[66:67], v[156:157], v[54:55] op_sel_hi:[1,0,1]
	v_add_f32_e32 v82, v82, v83
	v_pk_mul_f32 v[56:57], v[56:57], v[126:127]
	v_pk_mul_f32 v[34:35], v[44:45], v[126:127]
	v_add_f32_dpp v66, v82, v82 quad_perm:[1,0,3,2] row_mask:0xf bank_mask:0xf bound_ctrl:1
	v_pk_fma_f32 v[56:57], v[68:69], v[156:157], v[56:57] op_sel_hi:[1,0,1]
	v_pk_fma_f32 v[34:35], v[42:43], v[124:125], v[34:35]
	v_add_f32_dpp v66, v66, v66 quad_perm:[2,3,0,1] row_mask:0xf bank_mask:0xf bound_ctrl:1
	v_add_f32_e32 v168, v34, v35
	ds_read_b128 v[34:37], v150 offset:45824
	ds_read_b128 v[38:41], v150 offset:46080
	ds_read_b128 v[42:45], v150 offset:46336
	ds_read_b128 v[46:49], v150 offset:46592
	ds_read_b128 v[50:53], v150 offset:47104
	ds_read_b128 v[120:123], v150 offset:47360
	ds_read2st64_b32 v[158:159], v151 offset0:183 offset1:189
	v_add_f32_dpp v66, v66, v66 row_half_mirror row_mask:0xf bank_mask:0xf bound_ctrl:1
	s_nop 1
	v_add_f32_dpp v66, v66, v66 row_mirror row_mask:0xf bank_mask:0xf bound_ctrl:1
	v_pk_fma_f32 v[86:87], v[86:87], v[66:67], v[54:55] op_sel_hi:[1,0,1]
	v_pk_fma_f32 v[88:89], v[88:89], v[66:67], v[56:57] op_sel_hi:[1,0,1]
	s_waitcnt lgkmcnt(7)
	v_pk_mul_f32 v[78:79], v[78:79], v[86:87]
	v_pk_mul_f32 v[62:63], v[62:63], v[86:87]
	v_pk_fma_f32 v[78:79], v[80:81], v[88:89], v[78:79]
	v_pk_mul_f32 v[64:65], v[64:65], v[88:89]
	v_add_f32_e32 v79, v78, v79
	v_mov_b32_e32 v78, v157
	v_pk_fma_f32 v[62:63], v[74:75], v[78:79], v[62:63] op_sel_hi:[1,0,1]
	v_add_f32_dpp v74, v79, v79 quad_perm:[1,0,3,2] row_mask:0xf bank_mask:0xf bound_ctrl:1
	v_pk_fma_f32 v[64:65], v[76:77], v[78:79], v[64:65] op_sel_hi:[1,0,1]
	v_pk_mul_f32 v[54:55], v[60:61], v[88:89]
	v_add_f32_dpp v74, v74, v74 quad_perm:[2,3,0,1] row_mask:0xf bank_mask:0xf bound_ctrl:1
	v_pk_fma_f32 v[54:55], v[58:59], v[86:87], v[54:55]
	s_nop 0
	v_add_f32_dpp v74, v74, v74 row_half_mirror row_mask:0xf bank_mask:0xf bound_ctrl:1
	v_add_f32_e32 v124, v54, v55
	ds_read_b128 v[54:57], v150 offset:47616
	ds_read_b128 v[58:61], v150 offset:47872
	ds_read_b128 v[66:69], v150 offset:48128
	ds_read_b128 v[82:85], v150 offset:48640
	v_add_f32_dpp v74, v74, v74 row_mirror row_mask:0xf bank_mask:0xf bound_ctrl:1
	s_waitcnt lgkmcnt(10)
	v_pk_fma_f32 v[34:35], v[34:35], v[74:75], v[62:63] op_sel_hi:[1,0,1]
	v_pk_fma_f32 v[36:37], v[36:37], v[74:75], v[64:65] op_sel_hi:[1,0,1]
	s_waitcnt lgkmcnt(6)
	v_pk_mul_f32 v[50:51], v[50:51], v[34:35]
	v_pk_mul_f32 v[62:63], v[72:73], v[36:37]
	v_pk_fma_f32 v[50:51], v[52:53], v[36:37], v[50:51]
	v_pk_fma_f32 v[62:63], v[70:71], v[34:35], v[62:63]
	v_add_f32_e32 v50, v50, v51
	v_pk_mul_f32 v[34:35], v[38:39], v[34:35]
	v_pk_mul_f32 v[36:37], v[40:41], v[36:37]
	v_add_f32_dpp v38, v50, v50 quad_perm:[1,0,3,2] row_mask:0xf bank_mask:0xf bound_ctrl:1
	s_waitcnt lgkmcnt(4)
; #define LAS __attribute__((address_space(3)))
; #define SCAN_RS(N_, SEL_, CTRL_) _Pragma("unroll") for (int i = 0; i < (N_); ++i) { const float keep = (SEL_) ? yp[2 * i + 1] : yp[2 * i], send = (SEL_) ? yp[2 * i] : yp[2 * i + 1]; \
;                         yp[i] = keep + __builtin_bit_cast(float, __builtin_amdgcn_update_dpp(0, __builtin_bit_cast(int, send), (CTRL_), 0xF, 0xF, false)); }
; __device__ __forceinline__ void p5_scan_block(Frame& F, int sb) {
;     ...
;             for (int s = 0; s < SC_T; ++s) {
;                 f32x4 nw = w5, nr = r5, nk = k5, na = a5, nb = b5; float nv = v5;
;                 if (s + 2 < SC_T) { nw = *(const LAS f32x4*)(p + (s + 2) * 384); nr = *(const LAS f32x4*)(p + (s + 2) * 384 + 64); nk = *(const LAS f32x4*)(p + (s + 2) * 384 + 128);
;                     na = *(const LAS f32x4*)(p + (s + 2) * 384 + 256); nb = *(const LAS f32x4*)(p + (s + 2) * 384 + 320); nv = pv[(s + 2) * 384]; }
;                 const f32x2 pa = Sa * a4.lo + Sb * a4.hi;
;                 float sa = pa.x + pa.y;
;                 const f32x2 ta = Sa * w4.lo + k4.lo * vv, tb = Sb * w4.hi + k4.hi * vv;
;                 sa = dpp_add16(sa);
;                 Sa = ta + b4.lo * sa; Sb = tb + b4.hi * sa;
;                 const f32x2 py = Sa * r4.lo + Sb * r4.hi;
;                 yp[s & 15] = py.x + py.y;
;                 if ((s & 15) == 15) {
;     ...
;                     SCAN_RS(8, b3, 0x128) SCAN_RS(4, b2, 0x141) SCAN_RS(2, b1, 0x1B) SCAN_RS(1, b0, 0xB1)
;     ...
;                     yo[((s & 16) + qidx) * 16] = yp[0];
;                 }
	v_pk_fma_f32 v[36:37], v[48:49], v[158:159], v[36:37] op_sel_hi:[1,0,1]
	v_pk_fma_f32 v[34:35], v[46:47], v[158:159], v[34:35] op_sel_hi:[1,0,1]
	v_add_f32_dpp v38, v38, v38 quad_perm:[2,3,0,1] row_mask:0xf bank_mask:0xf bound_ctrl:1
	v_cndmask_b32_e64 v41, v165, v166, s[8:9]
	v_add_f32_e32 v62, v62, v63
	v_add_f32_dpp v38, v38, v38 row_half_mirror row_mask:0xf bank_mask:0xf bound_ctrl:1
	s_nop 1
	v_add_f32_dpp v38, v38, v38 row_mirror row_mask:0xf bank_mask:0xf bound_ctrl:1
	v_pk_fma_f32 v[36:37], v[122:123], v[38:39], v[36:37] op_sel_hi:[1,0,1]
	v_pk_fma_f32 v[34:35], v[120:121], v[38:39], v[34:35] op_sel_hi:[1,0,1]
	v_pk_mul_f32 v[38:39], v[44:45], v[36:37]
	s_nop 0
	v_pk_fma_f32 v[38:39], v[42:43], v[34:35], v[38:39]
	v_cndmask_b32_e64 v42, v167, v168, s[8:9]
	v_add_f32_e32 v40, v38, v39
	s_waitcnt lgkmcnt(0)
	v_pk_mul_f32 v[38:39], v[82:83], v[34:35]
	v_pk_mul_f32 v[34:35], v[54:55], v[34:35]
	v_pk_fma_f32 v[38:39], v[84:85], v[36:37], v[38:39]
	v_pk_mul_f32 v[36:37], v[56:57], v[36:37]
	v_add_f32_e32 v39, v38, v39
	v_mov_b32_e32 v38, v159
	v_pk_fma_f32 v[34:35], v[66:67], v[38:39], v[34:35] op_sel_hi:[1,0,1]
	v_pk_fma_f32 v[36:37], v[68:69], v[38:39], v[36:37] op_sel_hi:[1,0,1]
	v_add_f32_dpp v38, v39, v39 quad_perm:[1,0,3,2] row_mask:0xf bank_mask:0xf bound_ctrl:1
	v_cndmask_b32_e64 v43, v124, v62, s[8:9]
	s_nop 0
	v_add_f32_dpp v38, v38, v38 quad_perm:[2,3,0,1] row_mask:0xf bank_mask:0xf bound_ctrl:1
	s_nop 1
	v_add_f32_dpp v38, v38, v38 row_half_mirror row_mask:0xf bank_mask:0xf bound_ctrl:1
	s_nop 1
	v_add_f32_dpp v38, v38, v38 row_mirror row_mask:0xf bank_mask:0xf bound_ctrl:1
	v_pk_fma_f32 v[68:69], v[92:93], v[38:39], v[36:37] op_sel_hi:[1,0,1]
	v_pk_fma_f32 v[66:67], v[90:91], v[38:39], v[34:35] op_sel_hi:[1,0,1]
	v_pk_mul_f32 v[34:35], v[60:61], v[68:69]
	v_cndmask_b32_e64 v36, v153, v154, s[8:9]
	v_pk_fma_f32 v[34:35], v[58:59], v[66:67], v[34:35]
	v_cndmask_b32_e64 v37, v155, v160, s[8:9]
	v_add_f32_e32 v34, v34, v35
	v_cndmask_b32_e64 v35, v154, v153, s[8:9]
	v_cndmask_b32_e64 v38, v161, v162, s[8:9]
	v_cndmask_b32_e64 v39, v163, v164, s[8:9]
	v_add_f32_dpp v35, v36, v35 row_ror:8 row_mask:0xf bank_mask:0xf bound_ctrl:1
	v_cndmask_b32_e64 v36, v160, v155, s[8:9]
	s_nop 1
	v_add_f32_dpp v36, v37, v36 row_ror:8 row_mask:0xf bank_mask:0xf bound_ctrl:1
	v_cndmask_b32_e64 v37, v162, v161, s[8:9]
	s_nop 1
	v_add_f32_dpp v37, v38, v37 row_ror:8 row_mask:0xf bank_mask:0xf bound_ctrl:1
	v_cndmask_b32_e64 v38, v164, v163, s[8:9]
	s_nop 1
	v_add_f32_dpp v38, v39, v38 row_ror:8 row_mask:0xf bank_mask:0xf bound_ctrl:1
	v_cndmask_b32_e64 v39, v166, v165, s[8:9]
	s_nop 1
	v_add_f32_dpp v39, v41, v39 row_ror:8 row_mask:0xf bank_mask:0xf bound_ctrl:1
	v_cndmask_b32_e64 v41, v168, v167, s[8:9]
	s_nop 1
	v_add_f32_dpp v41, v42, v41 row_ror:8 row_mask:0xf bank_mask:0xf bound_ctrl:1
	v_cndmask_b32_e64 v42, v62, v124, s[8:9]
	s_nop 1
	v_add_f32_dpp v42, v43, v42 row_ror:8 row_mask:0xf bank_mask:0xf bound_ctrl:1
	v_cndmask_b32_e64 v43, v34, v40, s[8:9]
	v_cndmask_b32_e64 v34, v40, v34, s[8:9]
	v_cndmask_b32_e64 v40, v36, v35, s[6:7]
	v_cndmask_b32_e64 v35, v35, v36, s[6:7]
	v_cndmask_b32_e64 v36, v38, v37, s[6:7]
	v_cndmask_b32_e64 v37, v37, v38, s[6:7]
	v_add_f32_dpp v34, v34, v43 row_ror:8 row_mask:0xf bank_mask:0xf bound_ctrl:1
	v_cndmask_b32_e64 v38, v39, v41, s[6:7]
	v_add_f32_dpp v36, v37, v36 row_half_mirror row_mask:0xf bank_mask:0xf bound_ctrl:1
	v_cndmask_b32_e64 v37, v41, v39, s[6:7]
	v_add_f32_dpp v35, v35, v40 row_half_mirror row_mask:0xf bank_mask:0xf bound_ctrl:1
	s_nop 0
	v_add_f32_dpp v37, v38, v37 row_half_mirror row_mask:0xf bank_mask:0xf bound_ctrl:1
	v_cndmask_b32_e64 v38, v34, v42, s[6:7]
	v_cndmask_b32_e64 v34, v42, v34, s[6:7]
	s_nop 1
	v_add_f32_dpp v34, v34, v38 row_half_mirror row_mask:0xf bank_mask:0xf bound_ctrl:1
	v_cndmask_b32_e64 v38, v36, v35, s[4:5]
	v_cndmask_b32_e64 v35, v35, v36, s[4:5]
	v_cndmask_b32_e64 v36, v34, v37, s[4:5]
	v_cndmask_b32_e64 v34, v37, v34, s[4:5]
	v_add_f32_dpp v35, v35, v38 quad_perm:[3,2,1,0] row_mask:0xf bank_mask:0xf bound_ctrl:1
	s_nop 0
	v_add_f32_dpp v34, v34, v36 quad_perm:[3,2,1,0] row_mask:0xf bank_mask:0xf bound_ctrl:1
	v_cndmask_b32_e64 v36, v34, v35, s[0:1]
	v_cndmask_b32_e64 v34, v35, v34, s[0:1]
	s_nop 1
	v_add_f32_dpp v34, v34, v36 quad_perm:[1,0,3,2] row_mask:0xf bank_mask:0xf bound_ctrl:1
	ds_write_b32 v152, v34 offset:1024

; #define LAS __attribute__((address_space(3)))
; __device__ __forceinline__ void scan_flush_y(const LAS float* yb, float* Y, int c, int pt, int colbase) {
;     const LAS float* s = yb + (c & 1) * (SC_T * 16);
; #pragma unroll
;     for (int i = 0; i < 2; ++i) { const int idx = pt + 256 * i, st = idx >> 4, rr = idx & 15; Y[(size_t)(c * SC_T + st) * RW + colbase + rr] = s[idx]; }
; }
; __device__ __forceinline__ void p5_scan_block(Frame& F, int sb) {
;     ...
;     if (F.wave >= 4) scan_flush_y(yb, Y, NCH - 1, pt, colbase);
.LBB0_2826:
	s_setprio 0
	s_and_b64 vcc, exec, s[28:29]
	s_cbranch_vccz .LBB0_2828
	s_mov_b32 s31, 0
	s_lshl_b64 s[0:1], s[30:31], 2
	s_add_u32 s0, s68, s0
	s_addc_u32 s1, s69, s1
	v_lshlrev_b32_e32 v2, 2, v100
	v_mov_b32_e32 v3, 0
	v_lshl_add_u64 v[2:3], s[0:1], 0, v[2:3]
	s_mov_b64 s[0:1], 0x27400000
	v_lshl_add_u64 v[2:3], v[2:3], 0, s[0:1]
	s_add_i32 s0, 0, 0x18800
	v_lshl_add_u32 v1, v94, 2, s0
	ds_read_b32 v1, v1
	v_lshlrev_b64 v[4:5], 13, v[98:99]
	v_lshl_add_u64 v[4:5], v[2:3], 0, v[4:5]
	s_mov_b32 s1, 0x3fc0000
	v_add_co_u32_e32 v4, vcc, s1, v4
	v_lshl_add_u32 v6, v146, 2, s0
	s_nop 0
	v_addc_co_u32_e32 v5, vcc, 0, v5, vcc
	ds_read_b32 v6, v6
	s_waitcnt lgkmcnt(1)
	global_store_dword v[4:5], v1, off
	v_lshlrev_b64 v[4:5], 13, v[96:97]
	v_lshl_add_u64 v[2:3], v[2:3], 0, v[4:5]
	v_add_co_u32_e32 v2, vcc, 0x3fc0000, v2
	s_nop 1
	v_addc_co_u32_e32 v3, vcc, 0, v3, vcc
	s_waitcnt lgkmcnt(0)
	global_store_dword v[2:3], v6, off
